# out-projection and memory-output GEMM epilogues: residual-base loads issued up front instead of one load-wait-store ladder per row group
# baseline (speedup 1.0000x reference)
.LBB0_816:
	ds_read_b128 v[146:149], v152
	ds_read_b128 v[156:159], v152 offset:1024
	ds_read_b128 v[160:163], v152 offset:2048
	ds_read_b128 v[164:167], v152 offset:3072
	ds_read_b128 v[168:171], v153
	ds_read_b128 v[172:175], v153 offset:1024
	ds_read_b128 v[176:179], v153 offset:2048
	ds_read_b128 v[180:183], v153 offset:3072
	s_add_u32 s28, s26, 0xfff80080
	s_addc_u32 s29, s27, -1
	s_cmp_eq_u32 s54, 28
	s_cselect_b32 s31, s19, s29
	s_cselect_b32 s30, s25, s28
	s_cselect_b32 s29, s17, s53
	s_cselect_b32 s28, s51, s52
	v_lshl_add_u64 v[216:217], s[26:27], 0, v[138:139]
	s_add_i32 m0, s39, 0xc000
	ds_read_b128 v[184:187], v154
	ds_read_b128 v[188:191], v154 offset:1024
	ds_read_b128 v[192:195], v154 offset:2048
	ds_read_b128 v[196:199], v154 offset:3072
	ds_read_b128 v[200:203], v154 offset:4096
	ds_read_b128 v[204:207], v154 offset:5120
	ds_read_b128 v[208:211], v154 offset:6144
	ds_read_b128 v[212:215], v154 offset:7168
	global_load_lds_dwordx4 v[216:217], off
	v_lshl_add_u64 v[216:217], s[26:27], 0, v[140:141]
	s_add_i32 m0, s39, 0xe000
	s_nop 0
	global_load_lds_dwordx4 v[216:217], off
	s_waitcnt vmcnt(8)
	s_waitcnt lgkmcnt(0)
	s_barrier
	s_setprio 1
	s_waitcnt lgkmcnt(0)
	v_mfma_f32_16x16x32_bf16 v[126:129], v[146:149], v[184:187], v[126:129]
	v_mfma_f32_16x16x32_bf16 v[122:125], v[160:163], v[184:187], v[122:125]
	v_mfma_f32_16x16x32_bf16 v[110:113], v[146:149], v[192:195], v[110:113]
	v_mfma_f32_16x16x32_bf16 v[106:109], v[160:163], v[192:195], v[106:109]
	v_mfma_f32_16x16x32_bf16 v[94:97], v[146:149], v[200:203], v[94:97]
	v_mfma_f32_16x16x32_bf16 v[90:93], v[160:163], v[200:203], v[90:93]
	v_mfma_f32_16x16x32_bf16 v[78:81], v[146:149], v[208:211], v[78:81]
	v_mfma_f32_16x16x32_bf16 v[74:77], v[160:163], v[208:211], v[74:77]
	v_mfma_f32_16x16x32_bf16 v[126:129], v[156:159], v[188:191], v[126:129]
	v_mfma_f32_16x16x32_bf16 v[122:125], v[164:167], v[188:191], v[122:125]
	v_mfma_f32_16x16x32_bf16 v[110:113], v[156:159], v[196:199], v[110:113]
	v_mfma_f32_16x16x32_bf16 v[106:109], v[164:167], v[196:199], v[106:109]
	v_mfma_f32_16x16x32_bf16 v[94:97], v[156:159], v[204:207], v[94:97]
	v_mfma_f32_16x16x32_bf16 v[90:93], v[164:167], v[204:207], v[90:93]
	v_mfma_f32_16x16x32_bf16 v[78:81], v[156:159], v[212:215], v[78:81]
	v_mfma_f32_16x16x32_bf16 v[74:77], v[164:167], v[212:215], v[74:77]
	s_setprio 0
	s_setprio 1
	v_mfma_f32_16x16x32_bf16 v[118:121], v[168:171], v[184:187], v[118:121]
	v_mfma_f32_16x16x32_bf16 v[114:117], v[176:179], v[184:187], v[114:117]
	v_mfma_f32_16x16x32_bf16 v[102:105], v[168:171], v[192:195], v[102:105]
	v_mfma_f32_16x16x32_bf16 v[98:101], v[176:179], v[192:195], v[98:101]
	v_mfma_f32_16x16x32_bf16 v[86:89], v[168:171], v[200:203], v[86:89]
	v_mfma_f32_16x16x32_bf16 v[82:85], v[176:179], v[200:203], v[82:85]
	v_mfma_f32_16x16x32_bf16 v[70:73], v[168:171], v[208:211], v[70:73]
	v_mfma_f32_16x16x32_bf16 v[66:69], v[176:179], v[208:211], v[66:69]
	v_mfma_f32_16x16x32_bf16 v[118:121], v[172:175], v[188:191], v[118:121]
	v_mfma_f32_16x16x32_bf16 v[114:117], v[180:183], v[188:191], v[114:117]
	v_mfma_f32_16x16x32_bf16 v[102:105], v[172:175], v[196:199], v[102:105]
	v_mfma_f32_16x16x32_bf16 v[98:101], v[180:183], v[196:199], v[98:101]
	v_mfma_f32_16x16x32_bf16 v[86:89], v[172:175], v[204:207], v[86:89]
	v_mfma_f32_16x16x32_bf16 v[82:85], v[180:183], v[204:207], v[82:85]
	v_mfma_f32_16x16x32_bf16 v[70:73], v[172:175], v[212:215], v[70:73]
	v_mfma_f32_16x16x32_bf16 v[66:69], v[180:183], v[212:215], v[66:69]
	s_setprio 0
	s_barrier
	s_add_i32 s55, s48, s38
	v_lshl_add_u64 v[216:217], s[28:29], 0, v[132:133]
	s_mov_b32 m0, s55
	ds_read_b128 v[184:187], v154 offset:16384
	ds_read_b128 v[188:191], v154 offset:17408
	ds_read_b128 v[192:195], v154 offset:18432
	ds_read_b128 v[196:199], v154 offset:19456
	ds_read_b128 v[200:203], v154 offset:20480
	ds_read_b128 v[204:207], v154 offset:21504
	ds_read_b128 v[208:211], v154 offset:22528
	ds_read_b128 v[212:215], v154 offset:23552
	global_load_lds_dwordx4 v[216:217], off
	s_add_i32 m0, s55, 0x2000
	s_add_u32 s56, s28, 0x80000
	v_lshl_add_u64 v[218:219], s[28:29], 0, v[136:137]
	s_addc_u32 s57, s29, 0
	s_add_i32 s55, s49, s38
	global_load_lds_dwordx4 v[218:219], off
	v_lshl_add_u64 v[220:221], s[56:57], 0, v[132:133]
	s_mov_b32 m0, s55
	v_lshl_add_u64 v[222:223], s[30:31], 0, v[134:135]
	global_load_lds_dwordx4 v[220:221], off
	v_lshl_add_u64 v[220:221], s[56:57], 0, v[136:137]
	s_add_i32 m0, s55, 0x2000
	s_nop 0
	global_load_lds_dwordx4 v[220:221], off
	v_lshl_add_u64 v[220:221], s[30:31], 0, v[130:131]
	s_mov_b32 m0, s39
	s_nop 0
	global_load_lds_dwordx4 v[220:221], off
	s_mov_b32 m0, s40
	s_nop 0
	global_load_lds_dwordx4 v[222:223], off
	s_waitcnt vmcnt(8)
	s_waitcnt lgkmcnt(0)
	s_barrier
	s_setprio 1
	s_waitcnt lgkmcnt(0)
	v_mfma_f32_16x16x32_bf16 v[62:65], v[146:149], v[184:187], v[62:65]
	v_mfma_f32_16x16x32_bf16 v[58:61], v[160:163], v[184:187], v[58:61]
	v_mfma_f32_16x16x32_bf16 v[46:49], v[146:149], v[192:195], v[46:49]
	v_mfma_f32_16x16x32_bf16 v[42:45], v[160:163], v[192:195], v[42:45]
	v_mfma_f32_16x16x32_bf16 v[30:33], v[146:149], v[200:203], v[30:33]
	v_mfma_f32_16x16x32_bf16 v[26:29], v[160:163], v[200:203], v[26:29]
	v_mfma_f32_16x16x32_bf16 v[14:17], v[146:149], v[208:211], v[14:17]
	v_mfma_f32_16x16x32_bf16 v[10:13], v[160:163], v[208:211], v[10:13]
	v_mfma_f32_16x16x32_bf16 v[62:65], v[156:159], v[188:191], v[62:65]
	v_mfma_f32_16x16x32_bf16 v[58:61], v[164:167], v[188:191], v[58:61]
	v_mfma_f32_16x16x32_bf16 v[46:49], v[156:159], v[196:199], v[46:49]
	v_mfma_f32_16x16x32_bf16 v[42:45], v[164:167], v[196:199], v[42:45]
	v_mfma_f32_16x16x32_bf16 v[30:33], v[156:159], v[204:207], v[30:33]
	v_mfma_f32_16x16x32_bf16 v[26:29], v[164:167], v[204:207], v[26:29]
	v_mfma_f32_16x16x32_bf16 v[14:17], v[156:159], v[212:215], v[14:17]
	v_mfma_f32_16x16x32_bf16 v[10:13], v[164:167], v[212:215], v[10:13]
	s_setprio 0
	s_setprio 1
	v_mfma_f32_16x16x32_bf16 v[54:57], v[168:171], v[184:187], v[54:57]
	v_mfma_f32_16x16x32_bf16 v[50:53], v[176:179], v[184:187], v[50:53]
	v_mfma_f32_16x16x32_bf16 v[38:41], v[168:171], v[192:195], v[38:41]
	v_mfma_f32_16x16x32_bf16 v[34:37], v[176:179], v[192:195], v[34:37]
	v_mfma_f32_16x16x32_bf16 v[22:25], v[168:171], v[200:203], v[22:25]
	v_mfma_f32_16x16x32_bf16 v[18:21], v[176:179], v[200:203], v[18:21]
	v_mfma_f32_16x16x32_bf16 v[6:9], v[168:171], v[208:211], v[6:9]
	v_mfma_f32_16x16x32_bf16 v[2:5], v[176:179], v[208:211], v[2:5]
	v_mfma_f32_16x16x32_bf16 v[54:57], v[172:175], v[188:191], v[54:57]
	v_mfma_f32_16x16x32_bf16 v[50:53], v[180:183], v[188:191], v[50:53]
	v_mfma_f32_16x16x32_bf16 v[38:41], v[172:175], v[196:199], v[38:41]
	v_mfma_f32_16x16x32_bf16 v[34:37], v[180:183], v[196:199], v[34:37]
	v_mfma_f32_16x16x32_bf16 v[22:25], v[172:175], v[204:207], v[22:25]
	v_mfma_f32_16x16x32_bf16 v[18:21], v[180:183], v[204:207], v[18:21]
	v_mfma_f32_16x16x32_bf16 v[6:9], v[172:175], v[212:215], v[6:9]
	v_mfma_f32_16x16x32_bf16 v[2:5], v[180:183], v[212:215], v[2:5]
	s_setprio 0
	s_barrier
	s_add_i32 s55, 0, 0x18000
	s_add_i32 s56, 0, 0x1c000
	v_add_u32_e32 v164, s55, v150
	v_add_u32_e32 v180, s56, v150
	ds_read_b128 v[146:149], v164
	ds_read_b128 v[156:159], v164 offset:1024
	ds_read_b128 v[160:163], v164 offset:2048
	ds_read_b128 v[164:167], v164 offset:3072
	ds_read_b128 v[168:171], v180
	ds_read_b128 v[172:175], v180 offset:1024
	ds_read_b128 v[176:179], v180 offset:2048
	ds_read_b128 v[180:183], v180 offset:3072
	s_add_u32 s30, s30, 0x80000
	s_addc_u32 s31, s31, 0
	s_mov_b32 m0, s41
	v_lshl_add_u64 v[224:225], s[30:31], 0, v[130:131]
	ds_read_b128 v[184:187], v154 offset:32768
	ds_read_b128 v[188:191], v154 offset:33792
	ds_read_b128 v[192:195], v154 offset:34816
	ds_read_b128 v[196:199], v154 offset:35840
	ds_read_b128 v[200:203], v154 offset:36864
	ds_read_b128 v[204:207], v154 offset:37888
	ds_read_b128 v[208:211], v154 offset:38912
	ds_read_b128 v[212:215], v154 offset:39936
	global_load_lds_dwordx4 v[224:225], off
	v_lshl_add_u64 v[224:225], s[30:31], 0, v[134:135]
	s_mov_b32 m0, s42
	s_nop 0
	global_load_lds_dwordx4 v[224:225], off
	s_waitcnt vmcnt(8)
	s_waitcnt lgkmcnt(0)
	s_barrier
	s_setprio 1
	s_waitcnt lgkmcnt(0)
	v_mfma_f32_16x16x32_bf16 v[126:129], v[146:149], v[184:187], v[126:129]
	v_mfma_f32_16x16x32_bf16 v[122:125], v[160:163], v[184:187], v[122:125]
	v_mfma_f32_16x16x32_bf16 v[110:113], v[146:149], v[192:195], v[110:113]
	v_mfma_f32_16x16x32_bf16 v[106:109], v[160:163], v[192:195], v[106:109]
	v_mfma_f32_16x16x32_bf16 v[94:97], v[146:149], v[200:203], v[94:97]
	v_mfma_f32_16x16x32_bf16 v[90:93], v[160:163], v[200:203], v[90:93]
	v_mfma_f32_16x16x32_bf16 v[78:81], v[146:149], v[208:211], v[78:81]
	v_mfma_f32_16x16x32_bf16 v[74:77], v[160:163], v[208:211], v[74:77]
	v_mfma_f32_16x16x32_bf16 v[126:129], v[156:159], v[188:191], v[126:129]
	v_mfma_f32_16x16x32_bf16 v[122:125], v[164:167], v[188:191], v[122:125]
	v_mfma_f32_16x16x32_bf16 v[110:113], v[156:159], v[196:199], v[110:113]
	v_mfma_f32_16x16x32_bf16 v[106:109], v[164:167], v[196:199], v[106:109]
	v_mfma_f32_16x16x32_bf16 v[94:97], v[156:159], v[204:207], v[94:97]
	v_mfma_f32_16x16x32_bf16 v[90:93], v[164:167], v[204:207], v[90:93]
	v_mfma_f32_16x16x32_bf16 v[78:81], v[156:159], v[212:215], v[78:81]
	v_mfma_f32_16x16x32_bf16 v[74:77], v[164:167], v[212:215], v[74:77]
	s_setprio 0
	s_setprio 1
	v_mfma_f32_16x16x32_bf16 v[118:121], v[168:171], v[184:187], v[118:121]
	v_mfma_f32_16x16x32_bf16 v[114:117], v[176:179], v[184:187], v[114:117]
	v_mfma_f32_16x16x32_bf16 v[102:105], v[168:171], v[192:195], v[102:105]
	v_mfma_f32_16x16x32_bf16 v[98:101], v[176:179], v[192:195], v[98:101]
	v_mfma_f32_16x16x32_bf16 v[86:89], v[168:171], v[200:203], v[86:89]
	v_mfma_f32_16x16x32_bf16 v[82:85], v[176:179], v[200:203], v[82:85]
	v_mfma_f32_16x16x32_bf16 v[70:73], v[168:171], v[208:211], v[70:73]
	v_mfma_f32_16x16x32_bf16 v[66:69], v[176:179], v[208:211], v[66:69]
	v_mfma_f32_16x16x32_bf16 v[118:121], v[172:175], v[188:191], v[118:121]
	v_mfma_f32_16x16x32_bf16 v[114:117], v[180:183], v[188:191], v[114:117]
	v_mfma_f32_16x16x32_bf16 v[102:105], v[172:175], v[196:199], v[102:105]
	v_mfma_f32_16x16x32_bf16 v[98:101], v[180:183], v[196:199], v[98:101]
	v_mfma_f32_16x16x32_bf16 v[86:89], v[172:175], v[204:207], v[86:89]
	v_mfma_f32_16x16x32_bf16 v[82:85], v[180:183], v[204:207], v[82:85]
	v_mfma_f32_16x16x32_bf16 v[70:73], v[172:175], v[212:215], v[70:73]
	v_mfma_f32_16x16x32_bf16 v[66:69], v[180:183], v[212:215], v[66:69]
	s_setprio 0
	s_barrier
	s_add_i32 s30, s55, s38
	v_lshl_add_u64 v[216:217], v[216:217], 0, s[14:15]
	s_mov_b32 m0, s30
	ds_read_b128 v[184:187], v154 offset:49152
	ds_read_b128 v[188:191], v154 offset:50176
	ds_read_b128 v[192:195], v154 offset:51200
	ds_read_b128 v[196:199], v154 offset:52224
	ds_read_b128 v[200:203], v154 offset:53248
	ds_read_b128 v[204:207], v154 offset:54272
	ds_read_b128 v[208:211], v154 offset:55296
	ds_read_b128 v[212:215], v154 offset:56320
	global_load_lds_dwordx4 v[216:217], off
	s_add_i32 m0, s30, 0x2000
	s_add_u32 s28, s28, 0x80080
	v_lshl_add_u64 v[216:217], v[218:219], 0, s[14:15]
	s_addc_u32 s29, s29, 0
	s_add_i32 s30, s56, s38
	global_load_lds_dwordx4 v[216:217], off
	v_lshl_add_u64 v[216:217], s[28:29], 0, v[132:133]
	s_mov_b32 m0, s30
	s_nop 0
	global_load_lds_dwordx4 v[216:217], off
	v_lshl_add_u64 v[216:217], s[28:29], 0, v[136:137]
	s_add_i32 m0, s30, 0x2000
	s_nop 0
	global_load_lds_dwordx4 v[216:217], off
	v_lshl_add_u64 v[216:217], v[220:221], 0, s[14:15]
	s_mov_b32 m0, s44
	s_nop 0
	global_load_lds_dwordx4 v[216:217], off
	v_lshl_add_u64 v[216:217], v[222:223], 0, s[14:15]
	s_mov_b32 m0, s45
	s_nop 0
	global_load_lds_dwordx4 v[216:217], off
	s_waitcnt vmcnt(8)
	s_waitcnt lgkmcnt(0)
	s_barrier
	s_setprio 1
	s_waitcnt lgkmcnt(0)
	v_mfma_f32_16x16x32_bf16 v[62:65], v[146:149], v[184:187], v[62:65]
	v_mfma_f32_16x16x32_bf16 v[58:61], v[160:163], v[184:187], v[58:61]
	v_mfma_f32_16x16x32_bf16 v[46:49], v[146:149], v[192:195], v[46:49]
	v_mfma_f32_16x16x32_bf16 v[42:45], v[160:163], v[192:195], v[42:45]
	v_mfma_f32_16x16x32_bf16 v[30:33], v[146:149], v[200:203], v[30:33]
	v_mfma_f32_16x16x32_bf16 v[26:29], v[160:163], v[200:203], v[26:29]
	v_mfma_f32_16x16x32_bf16 v[14:17], v[146:149], v[208:211], v[14:17]
	v_mfma_f32_16x16x32_bf16 v[10:13], v[160:163], v[208:211], v[10:13]
	v_mfma_f32_16x16x32_bf16 v[62:65], v[156:159], v[188:191], v[62:65]
	v_mfma_f32_16x16x32_bf16 v[58:61], v[164:167], v[188:191], v[58:61]
	v_mfma_f32_16x16x32_bf16 v[46:49], v[156:159], v[196:199], v[46:49]
	v_mfma_f32_16x16x32_bf16 v[42:45], v[164:167], v[196:199], v[42:45]
	v_mfma_f32_16x16x32_bf16 v[30:33], v[156:159], v[204:207], v[30:33]
	v_mfma_f32_16x16x32_bf16 v[26:29], v[164:167], v[204:207], v[26:29]
	v_mfma_f32_16x16x32_bf16 v[14:17], v[156:159], v[212:215], v[14:17]
	v_mfma_f32_16x16x32_bf16 v[10:13], v[164:167], v[212:215], v[10:13]
	s_setprio 0
	s_setprio 1
	v_mfma_f32_16x16x32_bf16 v[54:57], v[168:171], v[184:187], v[54:57]
	v_mfma_f32_16x16x32_bf16 v[50:53], v[176:179], v[184:187], v[50:53]
	v_mfma_f32_16x16x32_bf16 v[38:41], v[168:171], v[192:195], v[38:41]
	v_mfma_f32_16x16x32_bf16 v[34:37], v[176:179], v[192:195], v[34:37]
	v_mfma_f32_16x16x32_bf16 v[22:25], v[168:171], v[200:203], v[22:25]
	v_mfma_f32_16x16x32_bf16 v[18:21], v[176:179], v[200:203], v[18:21]
	v_mfma_f32_16x16x32_bf16 v[6:9], v[168:171], v[208:211], v[6:9]
	v_mfma_f32_16x16x32_bf16 v[2:5], v[176:179], v[208:211], v[2:5]
	v_mfma_f32_16x16x32_bf16 v[54:57], v[172:175], v[188:191], v[54:57]
	v_mfma_f32_16x16x32_bf16 v[50:53], v[180:183], v[188:191], v[50:53]
	v_mfma_f32_16x16x32_bf16 v[38:41], v[172:175], v[196:199], v[38:41]
	v_mfma_f32_16x16x32_bf16 v[34:37], v[180:183], v[196:199], v[34:37]
	v_mfma_f32_16x16x32_bf16 v[22:25], v[172:175], v[204:207], v[22:25]
	v_mfma_f32_16x16x32_bf16 v[18:21], v[180:183], v[204:207], v[18:21]
	v_mfma_f32_16x16x32_bf16 v[6:9], v[172:175], v[212:215], v[6:9]
	v_mfma_f32_16x16x32_bf16 v[2:5], v[180:183], v[212:215], v[2:5]
	s_setprio 0
	s_barrier
	s_add_i32 s54, s54, 2
	s_add_u32 s26, s26, 0x100
	s_addc_u32 s27, s27, 0
	s_add_u32 s52, s52, 0x100
	s_addc_u32 s53, s53, 0
	s_cmp_gt_u32 s54, 29
	s_cbranch_scc0 .LBB0_816
	v_lshl_add_u32 v148, s24, 8, v1
	v_lshl_or_b32 v146, s6, 8, v151
	v_ashrrev_i32_e32 v149, 31, v148
	v_ashrrev_i32_e32 v147, 31, v146
	v_lshlrev_b64 v[156:157], 11, v[148:149]
	v_lshl_add_u64 v[164:165], v[156:157], 0, v[146:147]
	v_lshlrev_b64 v[166:167], 2, v[164:165]
	v_lshl_add_u64 v[168:169], s[72:73], 0, v[166:167]
	v_lshl_add_u64 v[142:143], s[72:73], 0, v[166:167]
	global_load_dwordx4 v[174:177], v[142:143], off
	global_load_dwordx4 v[178:181], v[142:143], off offset:16
	global_load_dwordx4 v[182:185], v[142:143], off offset:512
	global_load_dwordx4 v[186:189], v[142:143], off offset:528
	s_mov_b32 s98, 0x20000
	s_mov_b32 s99, 0
	v_lshl_add_u64 v[144:145], v[142:143], 0, s[98:99]
	global_load_dwordx4 v[190:193], v[144:145], off
	global_load_dwordx4 v[194:197], v[144:145], off offset:16
	global_load_dwordx4 v[198:201], v[144:145], off offset:512
	global_load_dwordx4 v[202:205], v[144:145], off offset:528
	s_mov_b32 s98, 0x40000
	s_mov_b32 s99, 0
	v_lshl_add_u64 v[144:145], v[142:143], 0, s[98:99]
	global_load_dwordx4 v[206:209], v[144:145], off
	global_load_dwordx4 v[210:213], v[144:145], off offset:16
	global_load_dwordx4 v[214:217], v[144:145], off offset:512
	global_load_dwordx4 v[218:221], v[144:145], off offset:528
	s_mov_b32 s98, 0x60000
	s_mov_b32 s99, 0
	v_lshl_add_u64 v[144:145], v[142:143], 0, s[98:99]
	global_load_dwordx4 v[222:225], v[144:145], off
	global_load_dwordx4 v[226:229], v[144:145], off offset:16
	global_load_dwordx4 v[230:233], v[144:145], off offset:512
	global_load_dwordx4 v[234:237], v[144:145], off offset:528
	s_mov_b32 s98, 0x100000
	s_mov_b32 s99, 0
	v_lshl_add_u64 v[144:145], v[142:143], 0, s[98:99]
	global_load_dwordx4 v[238:241], v[144:145], off
	global_load_dwordx4 v[242:245], v[144:145], off offset:16
	global_load_dwordx4 v[246:249], v[144:145], off offset:512
	global_load_dwordx4 v[250:253], v[144:145], off offset:528
	s_nop 0
	s_nop 0
	v_lshl_add_u64 v[170:171], v[164:165], 1, s[10:11]
	v_lshl_add_u64 v[172:173], s[8:9], 0, v[166:167]
	s_lshl_b32 s24, s6, 2
	s_ashr_i32 s25, s24, 31
	s_waitcnt vmcnt(19)
	v_pk_add_f32 v[128:129], v[128:129], v[176:177]
	v_pk_add_f32 v[126:127], v[126:127], v[174:175]
	s_waitcnt vmcnt(18)
	v_pk_add_f32 v[158:159], v[124:125], v[180:181]
	v_pk_add_f32 v[156:157], v[122:123], v[178:179]
	global_store_dwordx4 v[172:173], v[126:129], off
	global_store_dwordx4 v[172:173], v[156:159], off offset:16
	v_cvt_pk_bf16_f32 v122, v126, v127
	v_cvt_pk_bf16_f32 v123, v128, v129
	v_cvt_pk_bf16_f32 v124, v156, v157
	v_cvt_pk_bf16_f32 v125, v158, v159
	global_store_dwordx4 v[170:171], v[122:125], off
	s_nop 0
	s_nop 0
	v_mul_f32_e32 v124, v127, v127
	v_mul_f32_e32 v125, v129, v129
	v_mul_f32_e32 v127, v157, v157
	v_mul_f32_e32 v129, v159, v159
	v_fmac_f32_e32 v124, v126, v126
	v_fmac_f32_e32 v125, v128, v128
	v_fmac_f32_e32 v127, v156, v156
	v_fmac_f32_e32 v129, v158, v158
	v_add_f32_e32 v124, v124, v125
	v_add_f32_e32 v125, v127, v129
	v_add_f32_e32 v128, v124, v125
	v_and_b32_e32 v123, 64, v155
	v_xor_b32_e32 v122, 16, v155
	v_add_u32_e32 v123, 64, v123
	v_cmp_lt_i32_e32 vcc, v122, v123
	v_xor_b32_e32 v168, 32, v155
	s_waitcnt vmcnt(17)
	v_pk_add_f32 v[120:121], v[120:121], v[184:185]
	v_pk_add_f32 v[118:119], v[118:119], v[182:183]
	s_waitcnt vmcnt(16)
	v_pk_add_f32 v[126:127], v[116:117], v[188:189]
	v_pk_add_f32 v[124:125], v[114:115], v[186:187]
	s_mov_b32 s98, 0x120000
	s_mov_b32 s99, 0
	v_lshl_add_u64 v[144:145], v[142:143], 0, s[98:99]
	global_load_dwordx4 v[174:177], v[144:145], off
	global_load_dwordx4 v[178:181], v[144:145], off offset:16
	global_load_dwordx4 v[182:185], v[144:145], off offset:512
	global_load_dwordx4 v[186:189], v[144:145], off offset:528
	v_mul_f32_e32 v114, v119, v119
	v_mul_f32_e32 v115, v121, v121
	v_mul_f32_e32 v116, v125, v125
	v_mul_f32_e32 v117, v127, v127
	v_fmac_f32_e32 v114, v118, v118
	v_fmac_f32_e32 v115, v120, v120
	v_fmac_f32_e32 v116, v124, v124
	v_fmac_f32_e32 v117, v126, v126
	v_add_f32_e32 v114, v114, v115
	v_add_f32_e32 v115, v116, v117
	v_cndmask_b32_e32 v122, v155, v122, vcc
	v_add_f32_e32 v114, v114, v115
	v_lshlrev_b32_e32 v122, 2, v122
	v_add_f32_e32 v114, v128, v114
	ds_bpermute_b32 v115, v122, v114
	v_cmp_lt_i32_e32 vcc, v168, v123
	global_store_dwordx4 v[172:173], v[118:121], off offset:512
	global_store_dwordx4 v[172:173], v[124:127], off offset:528
	v_cndmask_b32_e32 v116, v155, v168, vcc
	v_lshlrev_b32_e32 v116, 2, v116
	s_waitcnt lgkmcnt(0)
	v_add_f32_e32 v114, v114, v115
	ds_bpermute_b32 v115, v116, v114
	v_cvt_pk_bf16_f32 v118, v118, v119
	v_cvt_pk_bf16_f32 v119, v120, v121
	v_cvt_pk_bf16_f32 v120, v124, v125
	v_cvt_pk_bf16_f32 v121, v126, v127
	global_store_dwordx4 v[170:171], v[118:121], off offset:256
	s_and_saveexec_b64 s[26:27], s[0:1]
	s_cbranch_execz .LBB0_819
	v_lshlrev_b64 v[118:119], 7, v[148:149]
	v_lshl_add_u64 v[118:119], s[12:13], 0, v[118:119]
	v_lshl_add_u64 v[118:119], s[24:25], 2, v[118:119]
	s_lshl_b32 s6, s43, 2
	v_lshl_add_u64 v[118:119], v[118:119], 0, s[6:7]
	s_waitcnt lgkmcnt(0)
	v_add_f32_e32 v114, v114, v115
	global_store_dword v[118:119], v114, off
.LBB0_819:
	s_or_b64 exec, exec, s[26:27]
	v_or_b32_e32 v114, 16, v148
	s_waitcnt lgkmcnt(0)
	v_ashrrev_i32_e32 v115, 31, v114
	v_lshlrev_b64 v[118:119], 11, v[114:115]
	v_lshl_add_u64 v[128:129], v[118:119], 0, v[146:147]
	v_lshlrev_b64 v[156:157], 2, v[128:129]
	v_lshl_add_u64 v[158:159], s[72:73], 0, v[156:157]
	s_nop 0
	s_nop 0
	v_lshl_add_u64 v[128:129], v[128:129], 1, s[10:11]
	v_lshl_add_u64 v[156:157], s[8:9], 0, v[156:157]
	s_waitcnt vmcnt(19)
	v_pk_add_f32 v[112:113], v[112:113], v[192:193]
	v_pk_add_f32 v[110:111], v[110:111], v[190:191]
	s_waitcnt vmcnt(18)
	v_pk_add_f32 v[108:109], v[108:109], v[196:197]
	v_pk_add_f32 v[106:107], v[106:107], v[194:195]
	global_store_dwordx4 v[156:157], v[110:113], off
	global_store_dwordx4 v[156:157], v[106:109], off offset:16
	v_cvt_pk_bf16_f32 v118, v110, v111
	v_cvt_pk_bf16_f32 v119, v112, v113
	v_cvt_pk_bf16_f32 v120, v106, v107
	v_cvt_pk_bf16_f32 v121, v108, v109
	global_store_dwordx4 v[128:129], v[118:121], off
	s_nop 0
	s_nop 0
	v_mul_f32_e32 v111, v111, v111
	v_mul_f32_e32 v113, v113, v113
	v_mul_f32_e32 v107, v107, v107
	v_mul_f32_e32 v109, v109, v109
	v_fmac_f32_e32 v111, v110, v110
	v_fmac_f32_e32 v113, v112, v112
	v_fmac_f32_e32 v107, v106, v106
	v_fmac_f32_e32 v109, v108, v108
	v_add_f32_e32 v106, v111, v113
	v_add_f32_e32 v107, v107, v109
	v_add_f32_e32 v110, v106, v107
	s_waitcnt vmcnt(17)
	v_pk_add_f32 v[104:105], v[104:105], v[200:201]
	v_pk_add_f32 v[102:103], v[102:103], v[198:199]
	s_waitcnt vmcnt(16)
	v_pk_add_f32 v[108:109], v[100:101], v[204:205]
	v_pk_add_f32 v[106:107], v[98:99], v[202:203]
	s_mov_b32 s98, 0x140000
	s_mov_b32 s99, 0
	v_lshl_add_u64 v[144:145], v[142:143], 0, s[98:99]
	global_load_dwordx4 v[190:193], v[144:145], off
	global_load_dwordx4 v[194:197], v[144:145], off offset:16
	global_load_dwordx4 v[198:201], v[144:145], off offset:512
	global_load_dwordx4 v[202:205], v[144:145], off offset:528
	v_mul_f32_e32 v98, v103, v103
	v_mul_f32_e32 v99, v105, v105
	v_mul_f32_e32 v100, v107, v107
	v_mul_f32_e32 v101, v109, v109
	v_fmac_f32_e32 v98, v102, v102
	v_fmac_f32_e32 v99, v104, v104
	v_fmac_f32_e32 v100, v106, v106
	v_fmac_f32_e32 v101, v108, v108
	v_add_f32_e32 v98, v98, v99
	v_add_f32_e32 v99, v100, v101
	v_add_f32_e32 v98, v98, v99
	v_add_f32_e32 v98, v110, v98
	ds_bpermute_b32 v99, v122, v98
	global_store_dwordx4 v[156:157], v[102:105], off offset:512
	global_store_dwordx4 v[156:157], v[106:109], off offset:528
	v_cvt_pk_bf16_f32 v100, v102, v103
	v_cvt_pk_bf16_f32 v101, v104, v105
	s_waitcnt lgkmcnt(0)
	v_add_f32_e32 v98, v98, v99
	ds_bpermute_b32 v99, v116, v98
	v_cvt_pk_bf16_f32 v102, v106, v107
	v_cvt_pk_bf16_f32 v103, v108, v109
	global_store_dwordx4 v[128:129], v[100:103], off offset:256
	s_and_saveexec_b64 s[26:27], s[0:1]
	s_cbranch_execz .LBB0_821
	v_lshlrev_b64 v[100:101], 7, v[114:115]
	v_lshl_add_u64 v[100:101], s[12:13], 0, v[100:101]
	v_lshl_add_u64 v[100:101], s[24:25], 2, v[100:101]
	s_lshl_b32 s6, s43, 2
	v_lshl_add_u64 v[100:101], v[100:101], 0, s[6:7]
	s_waitcnt lgkmcnt(0)
	v_add_f32_e32 v98, v98, v99
	global_store_dword v[100:101], v98, off
.LBB0_821:
	s_or_b64 exec, exec, s[26:27]
	v_or_b32_e32 v98, 32, v148
	s_waitcnt lgkmcnt(0)
	v_ashrrev_i32_e32 v99, 31, v98
	v_lshlrev_b64 v[100:101], 11, v[98:99]
	v_lshl_add_u64 v[108:109], v[100:101], 0, v[146:147]
	v_lshlrev_b64 v[110:111], 2, v[108:109]
	v_lshl_add_u64 v[112:113], s[72:73], 0, v[110:111]
	s_nop 0
	s_nop 0
	v_lshl_add_u64 v[108:109], v[108:109], 1, s[10:11]
	v_lshl_add_u64 v[110:111], s[8:9], 0, v[110:111]
	s_waitcnt vmcnt(19)
	v_pk_add_f32 v[96:97], v[96:97], v[208:209]
	v_pk_add_f32 v[94:95], v[94:95], v[206:207]
	s_waitcnt vmcnt(18)
	v_pk_add_f32 v[92:93], v[92:93], v[212:213]
	v_pk_add_f32 v[90:91], v[90:91], v[210:211]
	global_store_dwordx4 v[110:111], v[94:97], off
	global_store_dwordx4 v[110:111], v[90:93], off offset:16
	v_cvt_pk_bf16_f32 v100, v94, v95
	v_cvt_pk_bf16_f32 v101, v96, v97
	v_cvt_pk_bf16_f32 v102, v90, v91
	v_cvt_pk_bf16_f32 v103, v92, v93
	global_store_dwordx4 v[108:109], v[100:103], off
	s_nop 0
	s_nop 0
	v_mul_f32_e32 v95, v95, v95
	v_mul_f32_e32 v97, v97, v97
	v_mul_f32_e32 v91, v91, v91
	v_mul_f32_e32 v93, v93, v93
	v_fmac_f32_e32 v95, v94, v94
	v_fmac_f32_e32 v97, v96, v96
	v_fmac_f32_e32 v91, v90, v90
	v_fmac_f32_e32 v93, v92, v92
	v_add_f32_e32 v90, v95, v97
	v_add_f32_e32 v91, v91, v93
	v_add_f32_e32 v94, v90, v91
	s_waitcnt vmcnt(17)
	v_pk_add_f32 v[88:89], v[88:89], v[216:217]
	v_pk_add_f32 v[86:87], v[86:87], v[214:215]
	s_waitcnt vmcnt(16)
	v_pk_add_f32 v[92:93], v[84:85], v[220:221]
	v_pk_add_f32 v[90:91], v[82:83], v[218:219]
	s_mov_b32 s98, 0x160000
	s_mov_b32 s99, 0
	v_lshl_add_u64 v[144:145], v[142:143], 0, s[98:99]
	global_load_dwordx4 v[206:209], v[144:145], off
	global_load_dwordx4 v[210:213], v[144:145], off offset:16
	global_load_dwordx4 v[214:217], v[144:145], off offset:512
	global_load_dwordx4 v[218:221], v[144:145], off offset:528
	v_mul_f32_e32 v82, v87, v87
	v_mul_f32_e32 v83, v89, v89
	v_mul_f32_e32 v84, v91, v91
	v_mul_f32_e32 v85, v93, v93
	v_fmac_f32_e32 v82, v86, v86
	v_fmac_f32_e32 v83, v88, v88
	v_fmac_f32_e32 v84, v90, v90
	v_fmac_f32_e32 v85, v92, v92
	v_add_f32_e32 v82, v82, v83
	v_add_f32_e32 v83, v84, v85
	v_add_f32_e32 v82, v82, v83
	v_add_f32_e32 v82, v94, v82
	ds_bpermute_b32 v83, v122, v82
	global_store_dwordx4 v[110:111], v[86:89], off offset:512
	global_store_dwordx4 v[110:111], v[90:93], off offset:528
	v_cvt_pk_bf16_f32 v84, v86, v87
	v_cvt_pk_bf16_f32 v85, v88, v89
	s_waitcnt lgkmcnt(0)
	v_add_f32_e32 v82, v82, v83
	ds_bpermute_b32 v83, v116, v82
	v_cvt_pk_bf16_f32 v86, v90, v91
	v_cvt_pk_bf16_f32 v87, v92, v93
	global_store_dwordx4 v[108:109], v[84:87], off offset:256
	s_and_saveexec_b64 s[26:27], s[0:1]
	s_cbranch_execz .LBB0_823
	v_lshlrev_b64 v[84:85], 7, v[98:99]
	v_lshl_add_u64 v[84:85], s[12:13], 0, v[84:85]
	v_lshl_add_u64 v[84:85], s[24:25], 2, v[84:85]
	s_lshl_b32 s6, s43, 2
	v_lshl_add_u64 v[84:85], v[84:85], 0, s[6:7]
	s_waitcnt lgkmcnt(0)
	v_add_f32_e32 v82, v82, v83
	global_store_dword v[84:85], v82, off
.LBB0_823:
	s_or_b64 exec, exec, s[26:27]
	v_or_b32_e32 v82, 48, v148
	s_waitcnt lgkmcnt(0)
	v_ashrrev_i32_e32 v83, 31, v82
	v_lshlrev_b64 v[84:85], 11, v[82:83]
	v_lshl_add_u64 v[92:93], v[84:85], 0, v[146:147]
	v_lshlrev_b64 v[94:95], 2, v[92:93]
	v_lshl_add_u64 v[96:97], s[72:73], 0, v[94:95]
	s_nop 0
	s_nop 0
	v_lshl_add_u64 v[92:93], v[92:93], 1, s[10:11]
	v_lshl_add_u64 v[94:95], s[8:9], 0, v[94:95]
	s_waitcnt vmcnt(19)
	v_pk_add_f32 v[80:81], v[80:81], v[224:225]
	v_pk_add_f32 v[78:79], v[78:79], v[222:223]
	s_waitcnt vmcnt(18)
	v_pk_add_f32 v[76:77], v[76:77], v[228:229]
	v_pk_add_f32 v[74:75], v[74:75], v[226:227]
	global_store_dwordx4 v[94:95], v[78:81], off
	global_store_dwordx4 v[94:95], v[74:77], off offset:16
	v_cvt_pk_bf16_f32 v84, v78, v79
	v_cvt_pk_bf16_f32 v85, v80, v81
	v_cvt_pk_bf16_f32 v86, v74, v75
	v_cvt_pk_bf16_f32 v87, v76, v77
	global_store_dwordx4 v[92:93], v[84:87], off
	s_nop 0
	s_nop 0
	v_mul_f32_e32 v79, v79, v79
	v_mul_f32_e32 v81, v81, v81
	v_mul_f32_e32 v75, v75, v75
	v_mul_f32_e32 v77, v77, v77
	v_fmac_f32_e32 v79, v78, v78
	v_fmac_f32_e32 v81, v80, v80
	v_fmac_f32_e32 v75, v74, v74
	v_fmac_f32_e32 v77, v76, v76
	v_add_f32_e32 v74, v79, v81
	v_add_f32_e32 v75, v75, v77
	v_add_f32_e32 v78, v74, v75
	s_waitcnt vmcnt(17)
	v_pk_add_f32 v[72:73], v[72:73], v[232:233]
	v_pk_add_f32 v[70:71], v[70:71], v[230:231]
	s_waitcnt vmcnt(16)
	v_pk_add_f32 v[76:77], v[68:69], v[236:237]
	v_pk_add_f32 v[74:75], v[66:67], v[234:235]
	v_mul_f32_e32 v66, v71, v71
	v_mul_f32_e32 v67, v73, v73
	v_mul_f32_e32 v68, v75, v75
	v_mul_f32_e32 v69, v77, v77
	v_fmac_f32_e32 v66, v70, v70
	v_fmac_f32_e32 v67, v72, v72
	v_fmac_f32_e32 v68, v74, v74
	v_fmac_f32_e32 v69, v76, v76
	v_add_f32_e32 v66, v66, v67
	v_add_f32_e32 v67, v68, v69
	v_add_f32_e32 v66, v66, v67
	v_add_f32_e32 v66, v78, v66
	ds_bpermute_b32 v67, v122, v66
	global_store_dwordx4 v[94:95], v[70:73], off offset:512
	global_store_dwordx4 v[94:95], v[74:77], off offset:528
	v_cvt_pk_bf16_f32 v68, v70, v71
	v_cvt_pk_bf16_f32 v69, v72, v73
	s_waitcnt lgkmcnt(0)
	v_add_f32_e32 v66, v66, v67
	ds_bpermute_b32 v67, v116, v66
	v_cvt_pk_bf16_f32 v70, v74, v75
	v_cvt_pk_bf16_f32 v71, v76, v77
	global_store_dwordx4 v[92:93], v[68:71], off offset:256
	s_and_saveexec_b64 s[26:27], s[0:1]
	s_cbranch_execz .LBB0_825
	v_lshlrev_b64 v[68:69], 7, v[82:83]
	v_lshl_add_u64 v[68:69], s[12:13], 0, v[68:69]
	v_lshl_add_u64 v[68:69], s[24:25], 2, v[68:69]
	s_lshl_b32 s6, s43, 2
	v_lshl_add_u64 v[68:69], v[68:69], 0, s[6:7]
	s_waitcnt lgkmcnt(0)
	v_add_f32_e32 v66, v66, v67
	global_store_dword v[68:69], v66, off
.LBB0_825:
	s_or_b64 exec, exec, s[26:27]
	v_add_u32_e32 v66, 0x80, v148
	s_waitcnt lgkmcnt(0)
	v_ashrrev_i32_e32 v67, 31, v66
	v_lshlrev_b64 v[68:69], 11, v[66:67]
	v_lshl_add_u64 v[76:77], v[68:69], 0, v[146:147]
	v_lshlrev_b64 v[78:79], 2, v[76:77]
	v_lshl_add_u64 v[80:81], s[72:73], 0, v[78:79]
	s_nop 0
	s_nop 0
	v_lshl_add_u64 v[76:77], v[76:77], 1, s[10:11]
	v_lshl_add_u64 v[78:79], s[8:9], 0, v[78:79]
	s_waitcnt vmcnt(15)
	v_pk_add_f32 v[64:65], v[64:65], v[240:241]
	v_pk_add_f32 v[62:63], v[62:63], v[238:239]
	s_waitcnt vmcnt(14)
	v_pk_add_f32 v[60:61], v[60:61], v[244:245]
	v_pk_add_f32 v[58:59], v[58:59], v[242:243]
	global_store_dwordx4 v[78:79], v[62:65], off
	global_store_dwordx4 v[78:79], v[58:61], off offset:16
	v_cvt_pk_bf16_f32 v68, v62, v63
	v_cvt_pk_bf16_f32 v69, v64, v65
	v_cvt_pk_bf16_f32 v70, v58, v59
	v_cvt_pk_bf16_f32 v71, v60, v61
	global_store_dwordx4 v[76:77], v[68:71], off
	s_nop 0
	s_nop 0
	v_mul_f32_e32 v63, v63, v63
	v_mul_f32_e32 v65, v65, v65
	v_mul_f32_e32 v59, v59, v59
	v_mul_f32_e32 v61, v61, v61
	v_fmac_f32_e32 v63, v62, v62
	v_fmac_f32_e32 v65, v64, v64
	v_fmac_f32_e32 v59, v58, v58
	v_fmac_f32_e32 v61, v60, v60
	v_add_f32_e32 v58, v63, v65
	v_add_f32_e32 v59, v59, v61
	v_add_f32_e32 v62, v58, v59
	s_waitcnt vmcnt(13)
	v_pk_add_f32 v[56:57], v[56:57], v[248:249]
	v_pk_add_f32 v[54:55], v[54:55], v[246:247]
	s_waitcnt vmcnt(12)
	v_pk_add_f32 v[60:61], v[52:53], v[252:253]
	v_pk_add_f32 v[58:59], v[50:51], v[250:251]
	v_mul_f32_e32 v50, v55, v55
	v_mul_f32_e32 v51, v57, v57
	v_mul_f32_e32 v52, v59, v59
	v_mul_f32_e32 v53, v61, v61
	v_fmac_f32_e32 v50, v54, v54
	v_fmac_f32_e32 v51, v56, v56
	v_fmac_f32_e32 v52, v58, v58
	v_fmac_f32_e32 v53, v60, v60
	v_add_f32_e32 v50, v50, v51
	v_add_f32_e32 v51, v52, v53
	v_add_f32_e32 v50, v50, v51
	v_add_f32_e32 v50, v62, v50
	ds_bpermute_b32 v51, v122, v50
	global_store_dwordx4 v[78:79], v[54:57], off offset:512
	global_store_dwordx4 v[78:79], v[58:61], off offset:528
	v_cvt_pk_bf16_f32 v52, v54, v55
	v_cvt_pk_bf16_f32 v53, v56, v57
	s_waitcnt lgkmcnt(0)
	v_add_f32_e32 v50, v50, v51
	ds_bpermute_b32 v51, v116, v50
	v_cvt_pk_bf16_f32 v54, v58, v59
	v_cvt_pk_bf16_f32 v55, v60, v61
	global_store_dwordx4 v[76:77], v[52:55], off offset:256
	s_and_saveexec_b64 s[26:27], s[0:1]
	s_cbranch_execz .LBB0_827
	v_lshlrev_b64 v[52:53], 7, v[66:67]
	v_lshl_add_u64 v[52:53], s[12:13], 0, v[52:53]
	v_lshl_add_u64 v[52:53], s[24:25], 2, v[52:53]
	s_lshl_b32 s6, s43, 2
	v_lshl_add_u64 v[52:53], v[52:53], 0, s[6:7]
	s_waitcnt lgkmcnt(0)
	v_add_f32_e32 v50, v50, v51
	global_store_dword v[52:53], v50, off
.LBB0_827:
	s_or_b64 exec, exec, s[26:27]
	v_add_u32_e32 v50, 0x90, v148
	s_waitcnt lgkmcnt(0)
	v_ashrrev_i32_e32 v51, 31, v50
	v_lshlrev_b64 v[52:53], 11, v[50:51]
	v_lshl_add_u64 v[60:61], v[52:53], 0, v[146:147]
	v_lshlrev_b64 v[62:63], 2, v[60:61]
	v_lshl_add_u64 v[64:65], s[72:73], 0, v[62:63]
	s_nop 0
	s_nop 0
	v_lshl_add_u64 v[60:61], v[60:61], 1, s[10:11]
	v_lshl_add_u64 v[62:63], s[8:9], 0, v[62:63]
	s_waitcnt vmcnt(11)
	v_pk_add_f32 v[48:49], v[48:49], v[176:177]
	v_pk_add_f32 v[46:47], v[46:47], v[174:175]
	s_waitcnt vmcnt(10)
	v_pk_add_f32 v[44:45], v[44:45], v[180:181]
	v_pk_add_f32 v[42:43], v[42:43], v[178:179]
	global_store_dwordx4 v[62:63], v[46:49], off
	global_store_dwordx4 v[62:63], v[42:45], off offset:16
	v_cvt_pk_bf16_f32 v52, v46, v47
	v_cvt_pk_bf16_f32 v53, v48, v49
	v_cvt_pk_bf16_f32 v54, v42, v43
	v_cvt_pk_bf16_f32 v55, v44, v45
	global_store_dwordx4 v[60:61], v[52:55], off
	s_nop 0
	s_nop 0
	v_mul_f32_e32 v47, v47, v47
	v_mul_f32_e32 v49, v49, v49
	v_mul_f32_e32 v43, v43, v43
	v_mul_f32_e32 v45, v45, v45
	v_fmac_f32_e32 v47, v46, v46
	v_fmac_f32_e32 v49, v48, v48
	v_fmac_f32_e32 v43, v42, v42
	v_fmac_f32_e32 v45, v44, v44
	v_add_f32_e32 v42, v47, v49
	v_add_f32_e32 v43, v43, v45
	v_add_f32_e32 v46, v42, v43
	s_waitcnt vmcnt(9)
	v_pk_add_f32 v[40:41], v[40:41], v[184:185]
	v_pk_add_f32 v[38:39], v[38:39], v[182:183]
	s_waitcnt vmcnt(8)
	v_pk_add_f32 v[44:45], v[36:37], v[188:189]
	v_pk_add_f32 v[42:43], v[34:35], v[186:187]
	v_mul_f32_e32 v34, v39, v39
	v_mul_f32_e32 v35, v41, v41
	v_mul_f32_e32 v36, v43, v43
	v_mul_f32_e32 v37, v45, v45
	v_fmac_f32_e32 v34, v38, v38
	v_fmac_f32_e32 v35, v40, v40
	v_fmac_f32_e32 v36, v42, v42
	v_fmac_f32_e32 v37, v44, v44
	v_add_f32_e32 v34, v34, v35
	v_add_f32_e32 v35, v36, v37
	v_add_f32_e32 v34, v34, v35
	v_add_f32_e32 v34, v46, v34
	ds_bpermute_b32 v35, v122, v34
	global_store_dwordx4 v[62:63], v[38:41], off offset:512
	global_store_dwordx4 v[62:63], v[42:45], off offset:528
	v_cvt_pk_bf16_f32 v36, v38, v39
	v_cvt_pk_bf16_f32 v37, v40, v41
	s_waitcnt lgkmcnt(0)
	v_add_f32_e32 v34, v34, v35
	ds_bpermute_b32 v35, v116, v34
	v_cvt_pk_bf16_f32 v38, v42, v43
	v_cvt_pk_bf16_f32 v39, v44, v45
	global_store_dwordx4 v[60:61], v[36:39], off offset:256
	s_and_saveexec_b64 s[26:27], s[0:1]
	s_cbranch_execz .LBB0_829
	v_lshlrev_b64 v[36:37], 7, v[50:51]
	v_lshl_add_u64 v[36:37], s[12:13], 0, v[36:37]
	v_lshl_add_u64 v[36:37], s[24:25], 2, v[36:37]
	s_lshl_b32 s6, s43, 2
	v_lshl_add_u64 v[36:37], v[36:37], 0, s[6:7]
	s_waitcnt lgkmcnt(0)
	v_add_f32_e32 v34, v34, v35
	global_store_dword v[36:37], v34, off
.LBB0_829:
	s_or_b64 exec, exec, s[26:27]
	v_add_u32_e32 v34, 0xa0, v148
	s_waitcnt lgkmcnt(0)
	v_ashrrev_i32_e32 v35, 31, v34
	v_lshlrev_b64 v[36:37], 11, v[34:35]
	v_lshl_add_u64 v[44:45], v[36:37], 0, v[146:147]
	v_lshlrev_b64 v[46:47], 2, v[44:45]
	v_lshl_add_u64 v[48:49], s[72:73], 0, v[46:47]
	s_nop 0
	s_nop 0
	v_lshl_add_u64 v[44:45], v[44:45], 1, s[10:11]
	v_lshl_add_u64 v[46:47], s[8:9], 0, v[46:47]
	s_waitcnt vmcnt(7)
	v_pk_add_f32 v[32:33], v[32:33], v[192:193]
	v_pk_add_f32 v[30:31], v[30:31], v[190:191]
	s_waitcnt vmcnt(6)
	v_pk_add_f32 v[28:29], v[28:29], v[196:197]
	v_pk_add_f32 v[26:27], v[26:27], v[194:195]
	global_store_dwordx4 v[46:47], v[30:33], off
	global_store_dwordx4 v[46:47], v[26:29], off offset:16
	v_cvt_pk_bf16_f32 v36, v30, v31
	v_cvt_pk_bf16_f32 v37, v32, v33
	v_cvt_pk_bf16_f32 v38, v26, v27
	v_cvt_pk_bf16_f32 v39, v28, v29
	global_store_dwordx4 v[44:45], v[36:39], off
	s_nop 0
	s_nop 0
	v_mul_f32_e32 v31, v31, v31
	v_mul_f32_e32 v33, v33, v33
	v_mul_f32_e32 v27, v27, v27
	v_mul_f32_e32 v29, v29, v29
	v_fmac_f32_e32 v31, v30, v30
	v_fmac_f32_e32 v33, v32, v32
	v_fmac_f32_e32 v27, v26, v26
	v_fmac_f32_e32 v29, v28, v28
	v_add_f32_e32 v26, v31, v33
	v_add_f32_e32 v27, v27, v29
	v_add_f32_e32 v30, v26, v27
	s_waitcnt vmcnt(5)
	v_pk_add_f32 v[24:25], v[24:25], v[200:201]
	v_pk_add_f32 v[22:23], v[22:23], v[198:199]
	s_waitcnt vmcnt(4)
	v_pk_add_f32 v[28:29], v[20:21], v[204:205]
	v_pk_add_f32 v[26:27], v[18:19], v[202:203]
	v_mul_f32_e32 v18, v23, v23
	v_mul_f32_e32 v19, v25, v25
	v_mul_f32_e32 v20, v27, v27
	v_mul_f32_e32 v21, v29, v29
	v_fmac_f32_e32 v18, v22, v22
	v_fmac_f32_e32 v19, v24, v24
	v_fmac_f32_e32 v20, v26, v26
	v_fmac_f32_e32 v21, v28, v28
	v_add_f32_e32 v18, v18, v19
	v_add_f32_e32 v19, v20, v21
	v_add_f32_e32 v18, v18, v19
	v_add_f32_e32 v18, v30, v18
	ds_bpermute_b32 v19, v122, v18
	global_store_dwordx4 v[46:47], v[22:25], off offset:512
	global_store_dwordx4 v[46:47], v[26:29], off offset:528
	v_cvt_pk_bf16_f32 v20, v22, v23
	v_cvt_pk_bf16_f32 v21, v24, v25
	s_waitcnt lgkmcnt(0)
	v_add_f32_e32 v18, v18, v19
	ds_bpermute_b32 v19, v116, v18
	v_cvt_pk_bf16_f32 v22, v26, v27
	v_cvt_pk_bf16_f32 v23, v28, v29
	global_store_dwordx4 v[44:45], v[20:23], off offset:256
	s_and_saveexec_b64 s[26:27], s[0:1]
	s_cbranch_execz .LBB0_831
	v_lshlrev_b64 v[20:21], 7, v[34:35]
	v_lshl_add_u64 v[20:21], s[12:13], 0, v[20:21]
	v_lshl_add_u64 v[20:21], s[24:25], 2, v[20:21]
	s_lshl_b32 s6, s43, 2
	v_lshl_add_u64 v[20:21], v[20:21], 0, s[6:7]
	s_waitcnt lgkmcnt(0)
	v_add_f32_e32 v18, v18, v19
	global_store_dword v[20:21], v18, off
.LBB0_831:
	s_or_b64 exec, exec, s[26:27]
	v_add_u32_e32 v18, 0xb0, v148
	s_waitcnt lgkmcnt(0)
	v_ashrrev_i32_e32 v19, 31, v18
	v_lshlrev_b64 v[20:21], 11, v[18:19]
	v_lshl_add_u64 v[28:29], v[20:21], 0, v[146:147]
	v_lshlrev_b64 v[30:31], 2, v[28:29]
	v_lshl_add_u64 v[32:33], s[72:73], 0, v[30:31]
	s_nop 0
	s_nop 0
	v_lshl_add_u64 v[28:29], v[28:29], 1, s[10:11]
	v_lshl_add_u64 v[30:31], s[8:9], 0, v[30:31]
	s_waitcnt vmcnt(3)
	v_pk_add_f32 v[16:17], v[16:17], v[208:209]
	v_pk_add_f32 v[14:15], v[14:15], v[206:207]
	s_waitcnt vmcnt(2)
	v_pk_add_f32 v[12:13], v[12:13], v[212:213]
	v_pk_add_f32 v[10:11], v[10:11], v[210:211]
	global_store_dwordx4 v[30:31], v[14:17], off
	global_store_dwordx4 v[30:31], v[10:13], off offset:16
	v_cvt_pk_bf16_f32 v20, v14, v15
	v_cvt_pk_bf16_f32 v21, v16, v17
	v_cvt_pk_bf16_f32 v22, v10, v11
	v_cvt_pk_bf16_f32 v23, v12, v13
	global_store_dwordx4 v[28:29], v[20:23], off
	s_nop 0
	s_nop 0
	v_mul_f32_e32 v15, v15, v15
	v_mul_f32_e32 v17, v17, v17
	v_mul_f32_e32 v11, v11, v11
	v_mul_f32_e32 v13, v13, v13
	v_fmac_f32_e32 v15, v14, v14
	v_fmac_f32_e32 v17, v16, v16
	v_fmac_f32_e32 v11, v10, v10
	v_fmac_f32_e32 v13, v12, v12
	v_add_f32_e32 v10, v15, v17
	v_add_f32_e32 v11, v11, v13
	v_add_f32_e32 v14, v10, v11
	s_waitcnt vmcnt(1)
	v_pk_add_f32 v[8:9], v[8:9], v[216:217]
	v_pk_add_f32 v[6:7], v[6:7], v[214:215]
	s_waitcnt vmcnt(0)
	v_pk_add_f32 v[12:13], v[4:5], v[220:221]
	v_pk_add_f32 v[10:11], v[2:3], v[218:219]
	v_mul_f32_e32 v2, v7, v7
	v_mul_f32_e32 v3, v9, v9
	v_mul_f32_e32 v4, v11, v11
	v_mul_f32_e32 v5, v13, v13
	v_fmac_f32_e32 v2, v6, v6
	v_fmac_f32_e32 v3, v8, v8
	v_fmac_f32_e32 v4, v10, v10
	v_fmac_f32_e32 v5, v12, v12
	v_add_f32_e32 v2, v2, v3
	v_add_f32_e32 v3, v4, v5
	v_add_f32_e32 v2, v2, v3
	v_add_f32_e32 v2, v14, v2
	ds_bpermute_b32 v3, v122, v2
	global_store_dwordx4 v[30:31], v[6:9], off offset:512
	global_store_dwordx4 v[30:31], v[10:13], off offset:528
	v_cvt_pk_bf16_f32 v4, v6, v7
	v_cvt_pk_bf16_f32 v5, v8, v9
	s_waitcnt lgkmcnt(0)
	v_add_f32_e32 v2, v2, v3
	ds_bpermute_b32 v3, v116, v2
	v_cvt_pk_bf16_f32 v6, v10, v11
	v_cvt_pk_bf16_f32 v7, v12, v13
	global_store_dwordx4 v[28:29], v[4:7], off offset:256
	s_and_saveexec_b64 s[26:27], s[0:1]
	s_cbranch_execz .LBB0_808
	v_lshlrev_b64 v[4:5], 7, v[18:19]
	v_lshl_add_u64 v[4:5], s[12:13], 0, v[4:5]
	v_lshl_add_u64 v[4:5], s[24:25], 2, v[4:5]
	s_lshl_b32 s6, s43, 2
	v_lshl_add_u64 v[4:5], v[4:5], 0, s[6:7]
	s_waitcnt lgkmcnt(0)
	v_add_f32_e32 v2, v2, v3
	global_store_dword v[4:5], v2, off
	s_branch .LBB0_808

.LBB0_1019:
	ds_read_b128 v[150:153], v146
	ds_read_b128 v[154:157], v146 offset:1024
	ds_read_b128 v[158:161], v146 offset:2048
	ds_read_b128 v[162:165], v146 offset:3072
	ds_read_b128 v[166:169], v147
	ds_read_b128 v[170:173], v147 offset:1024
	ds_read_b128 v[174:177], v147 offset:2048
	ds_read_b128 v[178:181], v147 offset:3072
	s_add_u32 s30, s28, 0xfffc0080
	s_addc_u32 s31, s29, -1
	s_cmp_eq_u32 s56, 12
	s_cselect_b32 s35, s21, s31
	s_cselect_b32 s34, s52, s30
	s_cselect_b32 s31, s19, s55
	s_cselect_b32 s30, s53, s54
	v_lshl_add_u64 v[142:143], s[28:29], 0, v[134:135]
	s_add_i32 m0, s27, 0xc000
	ds_read_b128 v[182:185], v148
	ds_read_b128 v[186:189], v148 offset:1024
	ds_read_b128 v[190:193], v148 offset:2048
	ds_read_b128 v[194:197], v148 offset:3072
	ds_read_b128 v[198:201], v148 offset:4096
	ds_read_b128 v[202:205], v148 offset:5120
	ds_read_b128 v[206:209], v148 offset:6144
	ds_read_b128 v[210:213], v148 offset:7168
	global_load_lds_dwordx4 v[142:143], off
	v_lshl_add_u64 v[142:143], s[28:29], 0, v[136:137]
	s_add_i32 m0, s27, 0xe000
	s_nop 0
	global_load_lds_dwordx4 v[142:143], off
	s_waitcnt vmcnt(8)
	s_waitcnt lgkmcnt(0)
	s_barrier
	s_setprio 1
	s_waitcnt lgkmcnt(0)
	v_mfma_f32_16x16x32_bf16 v[126:129], v[150:153], v[182:185], v[126:129]
	v_mfma_f32_16x16x32_bf16 v[122:125], v[158:161], v[182:185], v[122:125]
	v_mfma_f32_16x16x32_bf16 v[110:113], v[150:153], v[190:193], v[110:113]
	v_mfma_f32_16x16x32_bf16 v[106:109], v[158:161], v[190:193], v[106:109]
	v_mfma_f32_16x16x32_bf16 v[94:97], v[150:153], v[198:201], v[94:97]
	v_mfma_f32_16x16x32_bf16 v[90:93], v[158:161], v[198:201], v[90:93]
	v_mfma_f32_16x16x32_bf16 v[78:81], v[150:153], v[206:209], v[78:81]
	v_mfma_f32_16x16x32_bf16 v[74:77], v[158:161], v[206:209], v[74:77]
	v_mfma_f32_16x16x32_bf16 v[126:129], v[154:157], v[186:189], v[126:129]
	v_mfma_f32_16x16x32_bf16 v[122:125], v[162:165], v[186:189], v[122:125]
	v_mfma_f32_16x16x32_bf16 v[110:113], v[154:157], v[194:197], v[110:113]
	v_mfma_f32_16x16x32_bf16 v[106:109], v[162:165], v[194:197], v[106:109]
	v_mfma_f32_16x16x32_bf16 v[94:97], v[154:157], v[202:205], v[94:97]
	v_mfma_f32_16x16x32_bf16 v[90:93], v[162:165], v[202:205], v[90:93]
	v_mfma_f32_16x16x32_bf16 v[78:81], v[154:157], v[210:213], v[78:81]
	v_mfma_f32_16x16x32_bf16 v[74:77], v[162:165], v[210:213], v[74:77]
	s_setprio 0
	s_setprio 1
	v_mfma_f32_16x16x32_bf16 v[118:121], v[166:169], v[182:185], v[118:121]
	v_mfma_f32_16x16x32_bf16 v[114:117], v[174:177], v[182:185], v[114:117]
	v_mfma_f32_16x16x32_bf16 v[102:105], v[166:169], v[190:193], v[102:105]
	v_mfma_f32_16x16x32_bf16 v[98:101], v[174:177], v[190:193], v[98:101]
	v_mfma_f32_16x16x32_bf16 v[86:89], v[166:169], v[198:201], v[86:89]
	v_mfma_f32_16x16x32_bf16 v[82:85], v[174:177], v[198:201], v[82:85]
	v_mfma_f32_16x16x32_bf16 v[70:73], v[166:169], v[206:209], v[70:73]
	v_mfma_f32_16x16x32_bf16 v[66:69], v[174:177], v[206:209], v[66:69]
	v_mfma_f32_16x16x32_bf16 v[118:121], v[170:173], v[186:189], v[118:121]
	v_mfma_f32_16x16x32_bf16 v[114:117], v[178:181], v[186:189], v[114:117]
	v_mfma_f32_16x16x32_bf16 v[102:105], v[170:173], v[194:197], v[102:105]
	v_mfma_f32_16x16x32_bf16 v[98:101], v[178:181], v[194:197], v[98:101]
	v_mfma_f32_16x16x32_bf16 v[86:89], v[170:173], v[202:205], v[86:89]
	v_mfma_f32_16x16x32_bf16 v[82:85], v[178:181], v[202:205], v[82:85]
	v_mfma_f32_16x16x32_bf16 v[70:73], v[170:173], v[210:213], v[70:73]
	v_mfma_f32_16x16x32_bf16 v[66:69], v[178:181], v[210:213], v[66:69]
	s_setprio 0
	s_barrier
	s_add_i32 s57, s49, s41
	v_lshl_add_u64 v[142:143], s[30:31], 0, v[130:131]
	s_mov_b32 m0, s57
	ds_read_b128 v[182:185], v148 offset:16384
	ds_read_b128 v[186:189], v148 offset:17408
	ds_read_b128 v[190:193], v148 offset:18432
	ds_read_b128 v[194:197], v148 offset:19456
	ds_read_b128 v[198:201], v148 offset:20480
	ds_read_b128 v[202:205], v148 offset:21504
	ds_read_b128 v[206:209], v148 offset:22528
	ds_read_b128 v[210:213], v148 offset:23552
	global_load_lds_dwordx4 v[142:143], off
	s_add_i32 m0, s57, 0x2000
	s_add_u32 s58, s30, 0x40000
	v_lshl_add_u64 v[214:215], s[30:31], 0, v[132:133]
	s_addc_u32 s59, s31, 0
	s_add_i32 s57, s50, s41
	global_load_lds_dwordx4 v[214:215], off
	v_lshl_add_u64 v[216:217], s[58:59], 0, v[130:131]
	s_mov_b32 m0, s57
	v_lshl_add_u64 v[218:219], s[34:35], 0, v[132:133]
	global_load_lds_dwordx4 v[216:217], off
	v_lshl_add_u64 v[216:217], s[58:59], 0, v[132:133]
	s_add_i32 m0, s57, 0x2000
	s_nop 0
	global_load_lds_dwordx4 v[216:217], off
	v_lshl_add_u64 v[216:217], s[34:35], 0, v[130:131]
	s_mov_b32 m0, s27
	s_nop 0
	global_load_lds_dwordx4 v[216:217], off
	s_mov_b32 m0, s42
	s_nop 0
	global_load_lds_dwordx4 v[218:219], off
	s_waitcnt vmcnt(8)
	s_waitcnt lgkmcnt(0)
	s_barrier
	s_setprio 1
	s_waitcnt lgkmcnt(0)
	v_mfma_f32_16x16x32_bf16 v[62:65], v[150:153], v[182:185], v[62:65]
	v_mfma_f32_16x16x32_bf16 v[58:61], v[158:161], v[182:185], v[58:61]
	v_mfma_f32_16x16x32_bf16 v[46:49], v[150:153], v[190:193], v[46:49]
	v_mfma_f32_16x16x32_bf16 v[42:45], v[158:161], v[190:193], v[42:45]
	v_mfma_f32_16x16x32_bf16 v[30:33], v[150:153], v[198:201], v[30:33]
	v_mfma_f32_16x16x32_bf16 v[26:29], v[158:161], v[198:201], v[26:29]
	v_mfma_f32_16x16x32_bf16 v[14:17], v[150:153], v[206:209], v[14:17]
	v_mfma_f32_16x16x32_bf16 v[10:13], v[158:161], v[206:209], v[10:13]
	v_mfma_f32_16x16x32_bf16 v[62:65], v[154:157], v[186:189], v[62:65]
	v_mfma_f32_16x16x32_bf16 v[58:61], v[162:165], v[186:189], v[58:61]
	v_mfma_f32_16x16x32_bf16 v[46:49], v[154:157], v[194:197], v[46:49]
	v_mfma_f32_16x16x32_bf16 v[42:45], v[162:165], v[194:197], v[42:45]
	v_mfma_f32_16x16x32_bf16 v[30:33], v[154:157], v[202:205], v[30:33]
	v_mfma_f32_16x16x32_bf16 v[26:29], v[162:165], v[202:205], v[26:29]
	v_mfma_f32_16x16x32_bf16 v[14:17], v[154:157], v[210:213], v[14:17]
	v_mfma_f32_16x16x32_bf16 v[10:13], v[162:165], v[210:213], v[10:13]
	s_setprio 0
	s_setprio 1
	v_mfma_f32_16x16x32_bf16 v[54:57], v[166:169], v[182:185], v[54:57]
	v_mfma_f32_16x16x32_bf16 v[50:53], v[174:177], v[182:185], v[50:53]
	v_mfma_f32_16x16x32_bf16 v[38:41], v[166:169], v[190:193], v[38:41]
	v_mfma_f32_16x16x32_bf16 v[34:37], v[174:177], v[190:193], v[34:37]
	v_mfma_f32_16x16x32_bf16 v[22:25], v[166:169], v[198:201], v[22:25]
	v_mfma_f32_16x16x32_bf16 v[18:21], v[174:177], v[198:201], v[18:21]
	v_mfma_f32_16x16x32_bf16 v[6:9], v[166:169], v[206:209], v[6:9]
	v_mfma_f32_16x16x32_bf16 v[2:5], v[174:177], v[206:209], v[2:5]
	v_mfma_f32_16x16x32_bf16 v[54:57], v[170:173], v[186:189], v[54:57]
	v_mfma_f32_16x16x32_bf16 v[50:53], v[178:181], v[186:189], v[50:53]
	v_mfma_f32_16x16x32_bf16 v[38:41], v[170:173], v[194:197], v[38:41]
	v_mfma_f32_16x16x32_bf16 v[34:37], v[178:181], v[194:197], v[34:37]
	v_mfma_f32_16x16x32_bf16 v[22:25], v[170:173], v[202:205], v[22:25]
	v_mfma_f32_16x16x32_bf16 v[18:21], v[178:181], v[202:205], v[18:21]
	v_mfma_f32_16x16x32_bf16 v[6:9], v[170:173], v[210:213], v[6:9]
	v_mfma_f32_16x16x32_bf16 v[2:5], v[178:181], v[210:213], v[2:5]
	s_setprio 0
	s_barrier
	s_add_i32 s57, 0, 0x18000
	v_add_u32_e32 v149, s57, v144
	s_add_i32 s58, 0, 0x1c000
	ds_read_b128 v[150:153], v149
	ds_read_b128 v[154:157], v149 offset:1024
	ds_read_b128 v[158:161], v149 offset:2048
	ds_read_b128 v[162:165], v149 offset:3072
	v_add_u32_e32 v149, s58, v144
	ds_read_b128 v[166:169], v149
	ds_read_b128 v[170:173], v149 offset:1024
	ds_read_b128 v[174:177], v149 offset:2048
	ds_read_b128 v[178:181], v149 offset:3072
	s_add_u32 s34, s34, 0x40000
	s_addc_u32 s35, s35, 0
	s_mov_b32 m0, s43
	v_lshl_add_u64 v[220:221], s[34:35], 0, v[130:131]
	ds_read_b128 v[182:185], v148 offset:32768
	ds_read_b128 v[186:189], v148 offset:33792
	ds_read_b128 v[190:193], v148 offset:34816
	ds_read_b128 v[194:197], v148 offset:35840
	ds_read_b128 v[198:201], v148 offset:36864
	ds_read_b128 v[202:205], v148 offset:37888
	ds_read_b128 v[206:209], v148 offset:38912
	ds_read_b128 v[210:213], v148 offset:39936
	global_load_lds_dwordx4 v[220:221], off
	v_lshl_add_u64 v[220:221], s[34:35], 0, v[132:133]
	s_mov_b32 m0, s44
	s_nop 0
	global_load_lds_dwordx4 v[220:221], off
	s_waitcnt vmcnt(8)
	s_waitcnt lgkmcnt(0)
	s_barrier
	s_setprio 1
	s_waitcnt lgkmcnt(0)
	v_mfma_f32_16x16x32_bf16 v[126:129], v[150:153], v[182:185], v[126:129]
	v_mfma_f32_16x16x32_bf16 v[122:125], v[158:161], v[182:185], v[122:125]
	v_mfma_f32_16x16x32_bf16 v[110:113], v[150:153], v[190:193], v[110:113]
	v_mfma_f32_16x16x32_bf16 v[106:109], v[158:161], v[190:193], v[106:109]
	v_mfma_f32_16x16x32_bf16 v[94:97], v[150:153], v[198:201], v[94:97]
	v_mfma_f32_16x16x32_bf16 v[90:93], v[158:161], v[198:201], v[90:93]
	v_mfma_f32_16x16x32_bf16 v[78:81], v[150:153], v[206:209], v[78:81]
	v_mfma_f32_16x16x32_bf16 v[74:77], v[158:161], v[206:209], v[74:77]
	v_mfma_f32_16x16x32_bf16 v[126:129], v[154:157], v[186:189], v[126:129]
	v_mfma_f32_16x16x32_bf16 v[122:125], v[162:165], v[186:189], v[122:125]
	v_mfma_f32_16x16x32_bf16 v[110:113], v[154:157], v[194:197], v[110:113]
	v_mfma_f32_16x16x32_bf16 v[106:109], v[162:165], v[194:197], v[106:109]
	v_mfma_f32_16x16x32_bf16 v[94:97], v[154:157], v[202:205], v[94:97]
	v_mfma_f32_16x16x32_bf16 v[90:93], v[162:165], v[202:205], v[90:93]
	v_mfma_f32_16x16x32_bf16 v[78:81], v[154:157], v[210:213], v[78:81]
	v_mfma_f32_16x16x32_bf16 v[74:77], v[162:165], v[210:213], v[74:77]
	s_setprio 0
	s_setprio 1
	v_mfma_f32_16x16x32_bf16 v[118:121], v[166:169], v[182:185], v[118:121]
	v_mfma_f32_16x16x32_bf16 v[114:117], v[174:177], v[182:185], v[114:117]
	v_mfma_f32_16x16x32_bf16 v[102:105], v[166:169], v[190:193], v[102:105]
	v_mfma_f32_16x16x32_bf16 v[98:101], v[174:177], v[190:193], v[98:101]
	v_mfma_f32_16x16x32_bf16 v[86:89], v[166:169], v[198:201], v[86:89]
	v_mfma_f32_16x16x32_bf16 v[82:85], v[174:177], v[198:201], v[82:85]
	v_mfma_f32_16x16x32_bf16 v[70:73], v[166:169], v[206:209], v[70:73]
	v_mfma_f32_16x16x32_bf16 v[66:69], v[174:177], v[206:209], v[66:69]
	v_mfma_f32_16x16x32_bf16 v[118:121], v[170:173], v[186:189], v[118:121]
	v_mfma_f32_16x16x32_bf16 v[114:117], v[178:181], v[186:189], v[114:117]
	v_mfma_f32_16x16x32_bf16 v[102:105], v[170:173], v[194:197], v[102:105]
	v_mfma_f32_16x16x32_bf16 v[98:101], v[178:181], v[194:197], v[98:101]
	v_mfma_f32_16x16x32_bf16 v[86:89], v[170:173], v[202:205], v[86:89]
	v_mfma_f32_16x16x32_bf16 v[82:85], v[178:181], v[202:205], v[82:85]
	v_mfma_f32_16x16x32_bf16 v[70:73], v[170:173], v[210:213], v[70:73]
	v_mfma_f32_16x16x32_bf16 v[66:69], v[178:181], v[210:213], v[66:69]
	s_setprio 0
	s_barrier
	s_add_i32 s34, s57, s41
	v_lshl_add_u64 v[142:143], v[142:143], 0, s[8:9]
	s_mov_b32 m0, s34
	ds_read_b128 v[182:185], v148 offset:49152
	ds_read_b128 v[186:189], v148 offset:50176
	ds_read_b128 v[190:193], v148 offset:51200
	ds_read_b128 v[194:197], v148 offset:52224
	ds_read_b128 v[198:201], v148 offset:53248
	ds_read_b128 v[202:205], v148 offset:54272
	ds_read_b128 v[206:209], v148 offset:55296
	ds_read_b128 v[210:213], v148 offset:56320
	global_load_lds_dwordx4 v[142:143], off
	s_add_i32 m0, s34, 0x2000
	s_add_u32 s30, s30, 0x40080
	v_lshl_add_u64 v[142:143], v[214:215], 0, s[8:9]
	s_addc_u32 s31, s31, 0
	s_add_i32 s34, s58, s41
	global_load_lds_dwordx4 v[142:143], off
	v_lshl_add_u64 v[142:143], s[30:31], 0, v[130:131]
	s_mov_b32 m0, s34
	s_nop 0
	global_load_lds_dwordx4 v[142:143], off
	v_lshl_add_u64 v[142:143], s[30:31], 0, v[132:133]
	s_add_i32 m0, s34, 0x2000
	s_nop 0
	global_load_lds_dwordx4 v[142:143], off
	v_lshl_add_u64 v[142:143], v[216:217], 0, s[8:9]
	s_mov_b32 m0, s46
	s_nop 0
	global_load_lds_dwordx4 v[142:143], off
	v_lshl_add_u64 v[142:143], v[218:219], 0, s[8:9]
	s_mov_b32 m0, s47
	s_nop 0
	global_load_lds_dwordx4 v[142:143], off
	s_waitcnt vmcnt(8)
	s_waitcnt lgkmcnt(0)
	s_barrier
	s_setprio 1
	s_waitcnt lgkmcnt(0)
	v_mfma_f32_16x16x32_bf16 v[62:65], v[150:153], v[182:185], v[62:65]
	v_mfma_f32_16x16x32_bf16 v[58:61], v[158:161], v[182:185], v[58:61]
	v_mfma_f32_16x16x32_bf16 v[46:49], v[150:153], v[190:193], v[46:49]
	v_mfma_f32_16x16x32_bf16 v[42:45], v[158:161], v[190:193], v[42:45]
	v_mfma_f32_16x16x32_bf16 v[30:33], v[150:153], v[198:201], v[30:33]
	v_mfma_f32_16x16x32_bf16 v[26:29], v[158:161], v[198:201], v[26:29]
	v_mfma_f32_16x16x32_bf16 v[14:17], v[150:153], v[206:209], v[14:17]
	v_mfma_f32_16x16x32_bf16 v[10:13], v[158:161], v[206:209], v[10:13]
	v_mfma_f32_16x16x32_bf16 v[62:65], v[154:157], v[186:189], v[62:65]
	v_mfma_f32_16x16x32_bf16 v[58:61], v[162:165], v[186:189], v[58:61]
	v_mfma_f32_16x16x32_bf16 v[46:49], v[154:157], v[194:197], v[46:49]
	v_mfma_f32_16x16x32_bf16 v[42:45], v[162:165], v[194:197], v[42:45]
	v_mfma_f32_16x16x32_bf16 v[30:33], v[154:157], v[202:205], v[30:33]
	v_mfma_f32_16x16x32_bf16 v[26:29], v[162:165], v[202:205], v[26:29]
	v_mfma_f32_16x16x32_bf16 v[14:17], v[154:157], v[210:213], v[14:17]
	v_mfma_f32_16x16x32_bf16 v[10:13], v[162:165], v[210:213], v[10:13]
	s_setprio 0
	s_setprio 1
	v_mfma_f32_16x16x32_bf16 v[54:57], v[166:169], v[182:185], v[54:57]
	v_mfma_f32_16x16x32_bf16 v[50:53], v[174:177], v[182:185], v[50:53]
	v_mfma_f32_16x16x32_bf16 v[38:41], v[166:169], v[190:193], v[38:41]
	v_mfma_f32_16x16x32_bf16 v[34:37], v[174:177], v[190:193], v[34:37]
	v_mfma_f32_16x16x32_bf16 v[22:25], v[166:169], v[198:201], v[22:25]
	v_mfma_f32_16x16x32_bf16 v[18:21], v[174:177], v[198:201], v[18:21]
	v_mfma_f32_16x16x32_bf16 v[6:9], v[166:169], v[206:209], v[6:9]
	v_mfma_f32_16x16x32_bf16 v[2:5], v[174:177], v[206:209], v[2:5]
	v_mfma_f32_16x16x32_bf16 v[54:57], v[170:173], v[186:189], v[54:57]
	v_mfma_f32_16x16x32_bf16 v[50:53], v[178:181], v[186:189], v[50:53]
	v_mfma_f32_16x16x32_bf16 v[38:41], v[170:173], v[194:197], v[38:41]
	v_mfma_f32_16x16x32_bf16 v[34:37], v[178:181], v[194:197], v[34:37]
	v_mfma_f32_16x16x32_bf16 v[22:25], v[170:173], v[202:205], v[22:25]
	v_mfma_f32_16x16x32_bf16 v[18:21], v[178:181], v[202:205], v[18:21]
	v_mfma_f32_16x16x32_bf16 v[6:9], v[170:173], v[210:213], v[6:9]
	v_mfma_f32_16x16x32_bf16 v[2:5], v[178:181], v[210:213], v[2:5]
	s_setprio 0
	s_barrier
	s_add_i32 s56, s56, 2
	s_add_u32 s28, s28, 0x100
	s_addc_u32 s29, s29, 0
	s_add_u32 s54, s54, 0x100
	s_addc_u32 s55, s55, 0
	s_cmp_gt_u32 s56, 13
	s_cbranch_scc0 .LBB0_1019
	v_lshl_add_u32 v166, s26, 8, v1
	v_lshl_or_b32 v168, s51, 8, v145
	v_ashrrev_i32_e32 v167, 31, v166
	v_ashrrev_i32_e32 v169, 31, v168
	v_lshlrev_b64 v[142:143], 11, v[166:167]
	v_lshl_add_u64 v[142:143], v[142:143], 0, v[168:169]
	v_lshlrev_b64 v[142:143], 2, v[142:143]
	v_lshl_add_u64 v[162:163], s[4:5], 0, v[142:143]
	v_lshl_add_u64 v[146:147], s[4:5], 0, v[142:143]
	global_load_dwordx4 v[176:179], v[146:147], off
	global_load_dwordx4 v[180:183], v[146:147], off offset:64
	global_load_dwordx4 v[184:187], v[146:147], off offset:512
	global_load_dwordx4 v[188:191], v[146:147], off offset:576
	s_mov_b32 s98, 0x20000
	s_mov_b32 s99, 0
	v_lshl_add_u64 v[148:149], v[146:147], 0, s[98:99]
	global_load_dwordx4 v[192:195], v[148:149], off
	global_load_dwordx4 v[196:199], v[148:149], off offset:64
	global_load_dwordx4 v[200:203], v[148:149], off offset:512
	global_load_dwordx4 v[204:207], v[148:149], off offset:576
	s_mov_b32 s98, 0x40000
	s_mov_b32 s99, 0
	v_lshl_add_u64 v[148:149], v[146:147], 0, s[98:99]
	global_load_dwordx4 v[208:211], v[148:149], off
	global_load_dwordx4 v[212:215], v[148:149], off offset:64
	global_load_dwordx4 v[216:219], v[148:149], off offset:512
	global_load_dwordx4 v[220:223], v[148:149], off offset:576
	s_mov_b32 s98, 0x60000
	s_mov_b32 s99, 0
	v_lshl_add_u64 v[148:149], v[146:147], 0, s[98:99]
	global_load_dwordx4 v[224:227], v[148:149], off
	global_load_dwordx4 v[228:231], v[148:149], off offset:64
	global_load_dwordx4 v[232:235], v[148:149], off offset:512
	global_load_dwordx4 v[236:239], v[148:149], off offset:576
	s_nop 0
	s_nop 0
	s_nop 0
	s_nop 0
	v_or_b32_e32 v170, 16, v166
	v_ashrrev_i32_e32 v171, 31, v170
	v_lshlrev_b64 v[170:171], 11, v[170:171]
	v_lshl_add_u64 v[170:171], v[170:171], 0, v[168:169]
	v_lshl_add_u64 v[172:173], s[6:7], 0, v[142:143]
	v_lshlrev_b64 v[170:171], 2, v[170:171]
	v_lshl_add_u64 v[174:175], s[4:5], 0, v[170:171]
	s_and_b64 vcc, exec, s[0:1]
	s_mov_b32 s51, s18
	s_mov_b32 s26, s20
	s_mov_b64 s[30:31], s[24:25]
	s_mov_b64 s[28:29], s[22:23]
	s_waitcnt vmcnt(15)
	v_pk_add_f32 v[128:129], v[128:129], v[178:179]
	v_pk_add_f32 v[126:127], v[126:127], v[176:177]
	s_waitcnt vmcnt(14)
	v_pk_add_f32 v[124:125], v[124:125], v[182:183]
	v_pk_add_f32 v[122:123], v[122:123], v[180:181]
	s_waitcnt vmcnt(13)
	v_pk_add_f32 v[120:121], v[120:121], v[186:187]
	v_pk_add_f32 v[118:119], v[118:119], v[184:185]
	s_waitcnt vmcnt(12)
	v_pk_add_f32 v[116:117], v[116:117], v[190:191]
	v_pk_add_f32 v[114:115], v[114:115], v[188:189]
	s_mov_b32 s98, 0x100000
	s_mov_b32 s99, 0
	v_lshl_add_u64 v[148:149], v[146:147], 0, s[98:99]
	global_load_dwordx4 v[176:179], v[148:149], off
	global_load_dwordx4 v[180:183], v[148:149], off offset:64
	global_load_dwordx4 v[184:187], v[148:149], off offset:512
	global_load_dwordx4 v[188:191], v[148:149], off offset:576
	global_store_dwordx4 v[172:173], v[126:129], off
	global_store_dwordx4 v[172:173], v[122:125], off offset:64
	global_store_dwordx4 v[172:173], v[118:121], off offset:512
	global_store_dwordx4 v[172:173], v[114:117], off offset:576
	s_nop 0
	s_nop 0
	s_nop 0
	s_nop 0
	v_or_b32_e32 v150, 32, v166
	v_ashrrev_i32_e32 v151, 31, v150
	v_lshlrev_b64 v[150:151], 11, v[150:151]
	v_lshl_add_u64 v[150:151], v[150:151], 0, v[168:169]
	v_lshlrev_b64 v[150:151], 2, v[150:151]
	v_lshl_add_u64 v[152:153], s[6:7], 0, v[170:171]
	v_lshl_add_u64 v[154:155], s[4:5], 0, v[150:151]
	s_waitcnt vmcnt(15)
	v_pk_add_f32 v[112:113], v[112:113], v[194:195]
	v_pk_add_f32 v[110:111], v[110:111], v[192:193]
	s_waitcnt vmcnt(14)
	v_pk_add_f32 v[108:109], v[108:109], v[198:199]
	v_pk_add_f32 v[106:107], v[106:107], v[196:197]
	s_waitcnt vmcnt(13)
	v_pk_add_f32 v[104:105], v[104:105], v[202:203]
	v_pk_add_f32 v[102:103], v[102:103], v[200:201]
	s_waitcnt vmcnt(12)
	v_pk_add_f32 v[100:101], v[100:101], v[206:207]
	v_pk_add_f32 v[98:99], v[98:99], v[204:205]
	s_mov_b32 s98, 0x120000
	s_mov_b32 s99, 0
	v_lshl_add_u64 v[148:149], v[146:147], 0, s[98:99]
	global_load_dwordx4 v[192:195], v[148:149], off
	global_load_dwordx4 v[196:199], v[148:149], off offset:64
	global_load_dwordx4 v[200:203], v[148:149], off offset:512
	global_load_dwordx4 v[204:207], v[148:149], off offset:576
	global_store_dwordx4 v[152:153], v[110:113], off
	global_store_dwordx4 v[152:153], v[106:109], off offset:64
	global_store_dwordx4 v[152:153], v[102:105], off offset:512
	global_store_dwordx4 v[152:153], v[98:101], off offset:576
	s_nop 0
	s_nop 0
	s_nop 0
	s_nop 0
	v_or_b32_e32 v114, 48, v166
	v_ashrrev_i32_e32 v115, 31, v114
	v_lshlrev_b64 v[114:115], 11, v[114:115]
	v_lshl_add_u64 v[114:115], v[114:115], 0, v[168:169]
	v_lshlrev_b64 v[114:115], 2, v[114:115]
	v_lshl_add_u64 v[116:117], s[6:7], 0, v[150:151]
	v_lshl_add_u64 v[118:119], s[4:5], 0, v[114:115]
	s_waitcnt vmcnt(15)
	v_pk_add_f32 v[96:97], v[96:97], v[210:211]
	v_pk_add_f32 v[94:95], v[94:95], v[208:209]
	s_waitcnt vmcnt(14)
	v_pk_add_f32 v[92:93], v[92:93], v[214:215]
	v_pk_add_f32 v[90:91], v[90:91], v[212:213]
	s_waitcnt vmcnt(13)
	v_pk_add_f32 v[88:89], v[88:89], v[218:219]
	v_pk_add_f32 v[86:87], v[86:87], v[216:217]
	s_waitcnt vmcnt(12)
	v_pk_add_f32 v[84:85], v[84:85], v[222:223]
	v_pk_add_f32 v[82:83], v[82:83], v[220:221]
	s_mov_b32 s98, 0x140000
	s_mov_b32 s99, 0
	v_lshl_add_u64 v[148:149], v[146:147], 0, s[98:99]
	global_load_dwordx4 v[208:211], v[148:149], off
	global_load_dwordx4 v[212:215], v[148:149], off offset:64
	global_load_dwordx4 v[216:219], v[148:149], off offset:512
	global_load_dwordx4 v[220:223], v[148:149], off offset:576
	global_store_dwordx4 v[116:117], v[94:97], off
	global_store_dwordx4 v[116:117], v[90:93], off offset:64
	global_store_dwordx4 v[116:117], v[86:89], off offset:512
	global_store_dwordx4 v[116:117], v[82:85], off offset:576
	s_nop 0
	s_nop 0
	s_nop 0
	s_nop 0
	v_lshl_add_u64 v[98:99], v[142:143], 0, s[10:11]
	v_lshl_add_u64 v[100:101], s[6:7], 0, v[114:115]
	v_lshl_add_u64 v[102:103], s[4:5], 0, v[98:99]
	s_waitcnt vmcnt(15)
	v_pk_add_f32 v[80:81], v[80:81], v[226:227]
	v_pk_add_f32 v[78:79], v[78:79], v[224:225]
	s_waitcnt vmcnt(14)
	v_pk_add_f32 v[76:77], v[76:77], v[230:231]
	v_pk_add_f32 v[74:75], v[74:75], v[228:229]
	s_waitcnt vmcnt(13)
	v_pk_add_f32 v[72:73], v[72:73], v[234:235]
	v_pk_add_f32 v[70:71], v[70:71], v[232:233]
	s_waitcnt vmcnt(12)
	v_pk_add_f32 v[68:69], v[68:69], v[238:239]
	v_pk_add_f32 v[66:67], v[66:67], v[236:237]
	s_mov_b32 s98, 0x160000
	s_mov_b32 s99, 0
	v_lshl_add_u64 v[148:149], v[146:147], 0, s[98:99]
	global_load_dwordx4 v[224:227], v[148:149], off
	global_load_dwordx4 v[228:231], v[148:149], off offset:64
	global_load_dwordx4 v[232:235], v[148:149], off offset:512
	global_load_dwordx4 v[236:239], v[148:149], off offset:576
	global_store_dwordx4 v[100:101], v[78:81], off
	global_store_dwordx4 v[100:101], v[74:77], off offset:64
	global_store_dwordx4 v[100:101], v[70:73], off offset:512
	global_store_dwordx4 v[100:101], v[66:69], off offset:576
	s_nop 0
	s_nop 0
	s_nop 0
	s_nop 0
	v_lshl_add_u64 v[82:83], v[142:143], 0, s[12:13]
	v_lshl_add_u64 v[84:85], s[6:7], 0, v[98:99]
	v_lshl_add_u64 v[86:87], s[4:5], 0, v[82:83]
	s_waitcnt vmcnt(15)
	v_pk_add_f32 v[64:65], v[64:65], v[178:179]
	v_pk_add_f32 v[62:63], v[62:63], v[176:177]
	s_waitcnt vmcnt(14)
	v_pk_add_f32 v[60:61], v[60:61], v[182:183]
	v_pk_add_f32 v[58:59], v[58:59], v[180:181]
	s_waitcnt vmcnt(13)
	v_pk_add_f32 v[56:57], v[56:57], v[186:187]
	v_pk_add_f32 v[54:55], v[54:55], v[184:185]
	s_waitcnt vmcnt(12)
	v_pk_add_f32 v[52:53], v[52:53], v[190:191]
	v_pk_add_f32 v[50:51], v[50:51], v[188:189]
	global_store_dwordx4 v[84:85], v[62:65], off
	global_store_dwordx4 v[84:85], v[58:61], off offset:64
	global_store_dwordx4 v[84:85], v[54:57], off offset:512
	global_store_dwordx4 v[84:85], v[50:53], off offset:576
	s_nop 0
	s_nop 0
	s_nop 0
	s_nop 0
	v_lshl_add_u64 v[66:67], v[142:143], 0, s[14:15]
	v_lshl_add_u64 v[68:69], s[6:7], 0, v[82:83]
	v_lshl_add_u64 v[70:71], s[4:5], 0, v[66:67]
	s_waitcnt vmcnt(11)
	v_pk_add_f32 v[48:49], v[48:49], v[194:195]
	v_pk_add_f32 v[46:47], v[46:47], v[192:193]
	s_waitcnt vmcnt(10)
	v_pk_add_f32 v[44:45], v[44:45], v[198:199]
	v_pk_add_f32 v[42:43], v[42:43], v[196:197]
	s_waitcnt vmcnt(9)
	v_pk_add_f32 v[40:41], v[40:41], v[202:203]
	v_pk_add_f32 v[38:39], v[38:39], v[200:201]
	s_waitcnt vmcnt(8)
	v_pk_add_f32 v[36:37], v[36:37], v[206:207]
	v_pk_add_f32 v[34:35], v[34:35], v[204:205]
	global_store_dwordx4 v[68:69], v[46:49], off
	global_store_dwordx4 v[68:69], v[42:45], off offset:64
	global_store_dwordx4 v[68:69], v[38:41], off offset:512
	global_store_dwordx4 v[68:69], v[34:37], off offset:576
	s_nop 0
	s_nop 0
	s_nop 0
	s_nop 0
	v_lshl_add_u64 v[50:51], v[142:143], 0, s[16:17]
	v_lshl_add_u64 v[52:53], s[6:7], 0, v[66:67]
	v_lshl_add_u64 v[54:55], s[4:5], 0, v[50:51]
	s_waitcnt vmcnt(7)
	v_pk_add_f32 v[32:33], v[32:33], v[210:211]
	v_pk_add_f32 v[30:31], v[30:31], v[208:209]
	s_waitcnt vmcnt(6)
	v_pk_add_f32 v[28:29], v[28:29], v[214:215]
	v_pk_add_f32 v[26:27], v[26:27], v[212:213]
	s_waitcnt vmcnt(5)
	v_pk_add_f32 v[24:25], v[24:25], v[218:219]
	v_pk_add_f32 v[22:23], v[22:23], v[216:217]
	s_waitcnt vmcnt(4)
	v_pk_add_f32 v[20:21], v[20:21], v[222:223]
	v_pk_add_f32 v[18:19], v[18:19], v[220:221]
	global_store_dwordx4 v[52:53], v[30:33], off
	global_store_dwordx4 v[52:53], v[26:29], off offset:64
	global_store_dwordx4 v[52:53], v[22:25], off offset:512
	global_store_dwordx4 v[52:53], v[18:21], off offset:576
	s_nop 0
	s_nop 0
	s_nop 0
	s_nop 0
	v_lshl_add_u64 v[34:35], s[6:7], 0, v[50:51]
	s_waitcnt vmcnt(3)
	v_pk_add_f32 v[16:17], v[16:17], v[226:227]
	v_pk_add_f32 v[14:15], v[14:15], v[224:225]
	s_waitcnt vmcnt(2)
	v_pk_add_f32 v[12:13], v[12:13], v[230:231]
	v_pk_add_f32 v[10:11], v[10:11], v[228:229]
	s_waitcnt vmcnt(1)
	v_pk_add_f32 v[8:9], v[8:9], v[234:235]
	v_pk_add_f32 v[6:7], v[6:7], v[232:233]
	s_waitcnt vmcnt(0)
	v_pk_add_f32 v[4:5], v[4:5], v[238:239]
	v_pk_add_f32 v[2:3], v[2:3], v[236:237]
	global_store_dwordx4 v[34:35], v[14:17], off
	global_store_dwordx4 v[34:35], v[10:13], off offset:64
	global_store_dwordx4 v[34:35], v[6:9], off offset:512
	global_store_dwordx4 v[34:35], v[2:5], off offset:576
	s_cbranch_vccz .LBB0_1012
	s_waitcnt vmcnt(0)
	s_cmpk_gt_u32 s3, 0xff
	s_cbranch_scc1 .LBB0_1023
	s_barrier
